# code placement: one s_nop in front of the MoE phase so its GEMM K-loop head moves from byte phase 4 to 0 (mod 8); everything else as v60
# speedup vs baseline: 1.0034x; 1.0034x over previous
.LBB0_1435:
	s_nop 0
	s_mov_b32 s0, s54
	s_cmp_gt_i32 s0, s18
	s_cbranch_scc1 .LBB0_1487
	s_mov_b32 s0, s55
	s_cmp_ge_i32 s18, s0
	s_cbranch_scc1 .LBB0_1486
	s_load_dwordx8 s[0:7], s[92:93], 0x110
	s_waitcnt lgkmcnt(0)
	s_add_i32 s0, s79, 12
	s_mov_b32 s1, s6
	s_cmp_gt_i32 s1, s0
	s_cbranch_scc1 .LBB0_1486
	s_load_dwordx8 s[4:11], s[92:93], 0x110
	s_waitcnt lgkmcnt(0)
	s_mov_b32 s1, s11
	s_cmp_ge_i32 s0, s1
	s_cbranch_scc1 .LBB0_1486
	s_waitcnt vmcnt(0)
	v_readlane_b32 s2, v252, 17
	v_readlane_b32 s3, v252, 18
	s_mov_b32 s0, -1
	s_andn2_b64 vcc, exec, s[2:3]
	s_waitcnt vmcnt(0)
	s_barrier
	s_cbranch_vccnz .LBB0_1485
	v_mbcnt_lo_u32_b32 v0, s0, 0
	v_mbcnt_hi_u32_b32 v0, s0, v0
	v_cmp_eq_u32_e32 vcc, 0, v0
	s_and_saveexec_b64 s[0:1], vcc
	s_cbranch_execz .LBB0_1484
	v_readlane_b32 s2, v252, 5
	v_readlane_b32 s4, v252, 7
	v_readlane_b32 s3, v252, 6
	s_waitcnt vmcnt(0) expcnt(0) lgkmcnt(0)
	v_mov_b32_e32 v0, s4
	ds_read_b32 v2, v0
	ds_read_b32 v0, v0 offset:4
	s_waitcnt lgkmcnt(1)
	v_cmp_ne_u32_e32 vcc, 0, v2
	s_cbranch_vccnz .LBB0_1455
	v_readlane_b32 s4, v252, 0
	v_readlane_b32 s5, v252, 1
	s_load_dwordx2 s[8:9], s[4:5], 0x4
	s_add_u32 s4, s2, 0x1000
	s_addc_u32 s5, s3, 0
	s_add_u32 s6, s2, 0x1100
	s_addc_u32 s7, s3, 0
	v_readlane_b32 s10, v252, 2
	s_waitcnt lgkmcnt(0)
	s_mul_i32 s30, s8, s10
	s_add_u32 s8, s2, 0x1200
	s_mul_i32 s30, s30, s9
	s_addc_u32 s9, s3, 0
	s_add_u32 s10, s2, 0x1300
	s_addc_u32 s11, s3, 0
	s_mov_b32 s31, 1
	s_mov_b64 s[12:13], 0
	s_branch .LBB0_1445
